# v32 stack + hand-written out-proj EpiRes2 epilogue (all residual loads up front, packed f32 fma, transposed coalesced stores), later loops kept at the same byte phase
# speedup vs baseline: 1.0066x; 1.0032x over previous
.LBB0_1726:
	s_add_u32 s6, s46, 0x1c00000
	s_addc_u32 s7, s47, 0
	s_lshl_b32 s4, s0, 8
	s_add_i32 s0, s4, s76
	s_lshl_b32 s5, s1, 5
	s_lshl_b32 s98, s10, 8
	s_or_b32 s5, s5, s98
	s_lshl_b32 s98, s1, 2
	v_lshl_add_u32 v249, v167, 4, s98
	v_or_b32_e32 v142, s0, v146
	v_lshrrev_b32_e32 v143, 1, v248
	v_and_or_b32 v143, v143, 24, s5
	v_mov_b32_e32 v246, v142
	v_mov_b32_e32 v247, 0
	v_lshl_add_u64 v[246:247], v[246:247], 2, s[6:7]
	v_lshlrev_b32_e32 v142, 11, v142
	v_lshl_add_u32 v142, v143, 1, v142
	v_mov_b32_e32 v143, 0
	v_lshl_add_u64 v[142:143], s[60:61], 0, v[142:143]
	s_mov_b32 s98, 0x8000
	s_mov_b32 s99, 0
	s_mov_b32 s100, 0x28000
	s_mov_b32 s101, 0
	global_load_dword v214, v[246:247], off
	global_load_dword v216, v[246:247], off offset:64
	global_load_dword v218, v[246:247], off offset:128
	global_load_dword v220, v[246:247], off offset:192
	global_load_dword v222, v[246:247], off offset:512
	global_load_dword v224, v[246:247], off offset:576
	global_load_dword v226, v[246:247], off offset:640
	global_load_dword v228, v[246:247], off offset:704
	global_load_dwordx4 v[150:153], v[142:143], off
	global_load_dwordx4 v[154:157], v[142:143], off offset:256
	v_lshl_add_u64 v[142:143], v[142:143], 0, s[98:99]
	global_load_dwordx4 v[158:161], v[142:143], off
	global_load_dwordx4 v[162:165], v[142:143], off offset:256
	v_lshl_add_u64 v[142:143], v[142:143], 0, s[98:99]
	global_load_dwordx4 v[166:169], v[142:143], off
	global_load_dwordx4 v[170:173], v[142:143], off offset:256
	v_lshl_add_u64 v[142:143], v[142:143], 0, s[98:99]
	global_load_dwordx4 v[174:177], v[142:143], off
	global_load_dwordx4 v[178:181], v[142:143], off offset:256
	v_lshl_add_u64 v[142:143], v[142:143], 0, s[100:101]
	global_load_dwordx4 v[182:185], v[142:143], off
	global_load_dwordx4 v[186:189], v[142:143], off offset:256
	v_lshl_add_u64 v[142:143], v[142:143], 0, s[98:99]
	global_load_dwordx4 v[190:193], v[142:143], off
	global_load_dwordx4 v[194:197], v[142:143], off offset:256
	v_lshl_add_u64 v[142:143], v[142:143], 0, s[98:99]
	global_load_dwordx4 v[198:201], v[142:143], off
	global_load_dwordx4 v[202:205], v[142:143], off offset:256
	v_lshl_add_u64 v[142:143], v[142:143], 0, s[98:99]
	global_load_dwordx4 v[206:209], v[142:143], off
	global_load_dwordx4 v[210:213], v[142:143], off offset:256
	v_lshrrev_b32_e32 v144, 2, v248
	v_and_b32_e32 v145, 3, v248
	v_lshlrev_b32_e32 v147, 6, v145
	v_lshl_add_u32 v147, v144, 2, v147
	v_add_u32_e32 v144, s0, v144
	v_lshl_or_b32 v145, v145, 3, s5
	v_lshlrev_b32_e32 v144, 11, v144
	v_lshl_add_u32 v144, v145, 1, v144
	v_mov_b32_e32 v145, 0
	v_lshl_add_u64 v[144:145], s[60:61], 0, v[144:145]
	v_xor_b32_e32 v148, 16, v248
	v_lshlrev_b32_e32 v148, 2, v148
	v_xor_b32_e32 v149, 32, v248
	v_lshlrev_b32_e32 v149, 2, v149
	s_mov_b32 s5, 0xffff0000
	s_barrier
	s_waitcnt vmcnt(15)
	v_lshlrev_b32_e32 v134, 16, v150
	v_and_b32_e32 v135, s5, v150
	v_lshlrev_b32_e32 v136, 16, v151
	v_and_b32_e32 v137, s5, v151
	v_lshlrev_b32_e32 v138, 16, v152
	v_and_b32_e32 v139, s5, v152
	v_lshlrev_b32_e32 v140, 16, v153
	v_and_b32_e32 v141, s5, v153
	v_pk_fma_f32 v[130:131], v[214:215], v[134:135], v[130:131] op_sel_hi:[0,1,1]
	v_pk_fma_f32 v[132:133], v[214:215], v[136:137], v[132:133] op_sel_hi:[0,1,1]
	v_pk_fma_f32 v[126:127], v[214:215], v[138:139], v[126:127] op_sel_hi:[0,1,1]
	v_pk_fma_f32 v[128:129], v[214:215], v[140:141], v[128:129] op_sel_hi:[0,1,1]
	v_pk_mul_f32 v[230:231], v[130:131], v[130:131]
	v_pk_fma_f32 v[230:231], v[132:133], v[132:133], v[230:231]
	v_pk_fma_f32 v[230:231], v[126:127], v[126:127], v[230:231]
	v_pk_fma_f32 v[230:231], v[128:129], v[128:129], v[230:231]
	v_cvt_pk_bf16_f32 v130, v130, v131
	v_cvt_pk_bf16_f32 v131, v132, v133
	v_cvt_pk_bf16_f32 v132, v126, v127
	v_cvt_pk_bf16_f32 v133, v128, v129
	ds_bpermute_b32 v130, v147, v130
	ds_bpermute_b32 v131, v147, v131
	ds_bpermute_b32 v132, v147, v132
	ds_bpermute_b32 v133, v147, v133
	s_waitcnt vmcnt(14)
	v_lshlrev_b32_e32 v134, 16, v154
	v_and_b32_e32 v135, s5, v154
	v_lshlrev_b32_e32 v136, 16, v155
	v_and_b32_e32 v137, s5, v155
	v_lshlrev_b32_e32 v138, 16, v156
	v_and_b32_e32 v139, s5, v156
	v_lshlrev_b32_e32 v140, 16, v157
	v_and_b32_e32 v141, s5, v157
	v_pk_fma_f32 v[122:123], v[214:215], v[134:135], v[122:123] op_sel_hi:[0,1,1]
	v_pk_fma_f32 v[124:125], v[214:215], v[136:137], v[124:125] op_sel_hi:[0,1,1]
	v_pk_fma_f32 v[118:119], v[214:215], v[138:139], v[118:119] op_sel_hi:[0,1,1]
	v_pk_fma_f32 v[120:121], v[214:215], v[140:141], v[120:121] op_sel_hi:[0,1,1]
	v_pk_fma_f32 v[230:231], v[122:123], v[122:123], v[230:231]
	v_pk_fma_f32 v[230:231], v[124:125], v[124:125], v[230:231]
	v_pk_fma_f32 v[230:231], v[118:119], v[118:119], v[230:231]
	v_pk_fma_f32 v[230:231], v[120:121], v[120:121], v[230:231]
	v_cvt_pk_bf16_f32 v122, v122, v123
	v_cvt_pk_bf16_f32 v123, v124, v125
	v_cvt_pk_bf16_f32 v124, v118, v119
	v_cvt_pk_bf16_f32 v125, v120, v121
	ds_bpermute_b32 v122, v147, v122
	ds_bpermute_b32 v123, v147, v123
	ds_bpermute_b32 v124, v147, v124
	ds_bpermute_b32 v125, v147, v125
	s_waitcnt lgkmcnt(4)
	global_store_dwordx4 v[144:145], v[130:133], off
	s_waitcnt vmcnt(14)
	v_lshlrev_b32_e32 v134, 16, v158
	v_and_b32_e32 v135, s5, v158
	v_lshlrev_b32_e32 v136, 16, v159
	v_and_b32_e32 v137, s5, v159
	v_lshlrev_b32_e32 v138, 16, v160
	v_and_b32_e32 v139, s5, v160
	v_lshlrev_b32_e32 v140, 16, v161
	v_and_b32_e32 v141, s5, v161
	v_pk_fma_f32 v[114:115], v[216:217], v[134:135], v[114:115] op_sel_hi:[0,1,1]
	v_pk_fma_f32 v[116:117], v[216:217], v[136:137], v[116:117] op_sel_hi:[0,1,1]
	v_pk_fma_f32 v[106:107], v[216:217], v[138:139], v[106:107] op_sel_hi:[0,1,1]
	v_pk_fma_f32 v[108:109], v[216:217], v[140:141], v[108:109] op_sel_hi:[0,1,1]
	v_pk_mul_f32 v[232:233], v[114:115], v[114:115]
	v_pk_fma_f32 v[232:233], v[116:117], v[116:117], v[232:233]
	v_pk_fma_f32 v[232:233], v[106:107], v[106:107], v[232:233]
	v_pk_fma_f32 v[232:233], v[108:109], v[108:109], v[232:233]
	v_cvt_pk_bf16_f32 v114, v114, v115
	v_cvt_pk_bf16_f32 v115, v116, v117
	v_cvt_pk_bf16_f32 v116, v106, v107
	v_cvt_pk_bf16_f32 v117, v108, v109
	ds_bpermute_b32 v114, v147, v114
	ds_bpermute_b32 v115, v147, v115
	ds_bpermute_b32 v116, v147, v116
	ds_bpermute_b32 v117, v147, v117
	s_waitcnt lgkmcnt(4)
	global_store_dwordx4 v[144:145], v[122:125], off offset:256
	v_lshl_add_u64 v[144:145], v[144:145], 0, s[98:99]
	s_waitcnt vmcnt(14)
	v_lshlrev_b32_e32 v134, 16, v162
	v_and_b32_e32 v135, s5, v162
	v_lshlrev_b32_e32 v136, 16, v163
	v_and_b32_e32 v137, s5, v163
	v_lshlrev_b32_e32 v138, 16, v164
	v_and_b32_e32 v139, s5, v164
	v_lshlrev_b32_e32 v140, 16, v165
	v_and_b32_e32 v141, s5, v165
	v_pk_fma_f32 v[102:103], v[216:217], v[134:135], v[102:103] op_sel_hi:[0,1,1]
	v_pk_fma_f32 v[104:105], v[216:217], v[136:137], v[104:105] op_sel_hi:[0,1,1]
	v_pk_fma_f32 v[98:99], v[216:217], v[138:139], v[98:99] op_sel_hi:[0,1,1]
	v_pk_fma_f32 v[100:101], v[216:217], v[140:141], v[100:101] op_sel_hi:[0,1,1]
	v_pk_fma_f32 v[232:233], v[102:103], v[102:103], v[232:233]
	v_pk_fma_f32 v[232:233], v[104:105], v[104:105], v[232:233]
	v_pk_fma_f32 v[232:233], v[98:99], v[98:99], v[232:233]
	v_pk_fma_f32 v[232:233], v[100:101], v[100:101], v[232:233]
	v_cvt_pk_bf16_f32 v102, v102, v103
	v_cvt_pk_bf16_f32 v103, v104, v105
	v_cvt_pk_bf16_f32 v104, v98, v99
	v_cvt_pk_bf16_f32 v105, v100, v101
	ds_bpermute_b32 v102, v147, v102
	ds_bpermute_b32 v103, v147, v103
	ds_bpermute_b32 v104, v147, v104
	ds_bpermute_b32 v105, v147, v105
	s_waitcnt lgkmcnt(4)
	global_store_dwordx4 v[144:145], v[114:117], off
	s_waitcnt vmcnt(14)
	v_lshlrev_b32_e32 v134, 16, v166
	v_and_b32_e32 v135, s5, v166
	v_lshlrev_b32_e32 v136, 16, v167
	v_and_b32_e32 v137, s5, v167
	v_lshlrev_b32_e32 v138, 16, v168
	v_and_b32_e32 v139, s5, v168
	v_lshlrev_b32_e32 v140, 16, v169
	v_and_b32_e32 v141, s5, v169
	v_pk_fma_f32 v[94:95], v[218:219], v[134:135], v[94:95] op_sel_hi:[0,1,1]
	v_pk_fma_f32 v[96:97], v[218:219], v[136:137], v[96:97] op_sel_hi:[0,1,1]
	v_pk_fma_f32 v[90:91], v[218:219], v[138:139], v[90:91] op_sel_hi:[0,1,1]
	v_pk_fma_f32 v[92:93], v[218:219], v[140:141], v[92:93] op_sel_hi:[0,1,1]
	v_pk_mul_f32 v[234:235], v[94:95], v[94:95]
	v_pk_fma_f32 v[234:235], v[96:97], v[96:97], v[234:235]
	v_pk_fma_f32 v[234:235], v[90:91], v[90:91], v[234:235]
	v_pk_fma_f32 v[234:235], v[92:93], v[92:93], v[234:235]
	v_cvt_pk_bf16_f32 v94, v94, v95
	v_cvt_pk_bf16_f32 v95, v96, v97
	v_cvt_pk_bf16_f32 v96, v90, v91
	v_cvt_pk_bf16_f32 v97, v92, v93
	ds_bpermute_b32 v94, v147, v94
	ds_bpermute_b32 v95, v147, v95
	ds_bpermute_b32 v96, v147, v96
	ds_bpermute_b32 v97, v147, v97
	s_waitcnt lgkmcnt(4)
	global_store_dwordx4 v[144:145], v[102:105], off offset:256
	v_lshl_add_u64 v[144:145], v[144:145], 0, s[98:99]
	s_waitcnt vmcnt(14)
	v_lshlrev_b32_e32 v134, 16, v170
	v_and_b32_e32 v135, s5, v170
	v_lshlrev_b32_e32 v136, 16, v171
	v_and_b32_e32 v137, s5, v171
	v_lshlrev_b32_e32 v138, 16, v172
	v_and_b32_e32 v139, s5, v172
	v_lshlrev_b32_e32 v140, 16, v173
	v_and_b32_e32 v141, s5, v173
	v_pk_fma_f32 v[86:87], v[218:219], v[134:135], v[86:87] op_sel_hi:[0,1,1]
	v_pk_fma_f32 v[88:89], v[218:219], v[136:137], v[88:89] op_sel_hi:[0,1,1]
	v_pk_fma_f32 v[82:83], v[218:219], v[138:139], v[82:83] op_sel_hi:[0,1,1]
	v_pk_fma_f32 v[84:85], v[218:219], v[140:141], v[84:85] op_sel_hi:[0,1,1]
	v_pk_fma_f32 v[234:235], v[86:87], v[86:87], v[234:235]
	v_pk_fma_f32 v[234:235], v[88:89], v[88:89], v[234:235]
	v_pk_fma_f32 v[234:235], v[82:83], v[82:83], v[234:235]
	v_pk_fma_f32 v[234:235], v[84:85], v[84:85], v[234:235]
	v_cvt_pk_bf16_f32 v86, v86, v87
	v_cvt_pk_bf16_f32 v87, v88, v89
	v_cvt_pk_bf16_f32 v88, v82, v83
	v_cvt_pk_bf16_f32 v89, v84, v85
	ds_bpermute_b32 v86, v147, v86
	ds_bpermute_b32 v87, v147, v87
	ds_bpermute_b32 v88, v147, v88
	ds_bpermute_b32 v89, v147, v89
	s_waitcnt lgkmcnt(4)
	global_store_dwordx4 v[144:145], v[94:97], off
	s_waitcnt vmcnt(14)
	v_lshlrev_b32_e32 v134, 16, v174
	v_and_b32_e32 v135, s5, v174
	v_lshlrev_b32_e32 v136, 16, v175
	v_and_b32_e32 v137, s5, v175
	v_lshlrev_b32_e32 v138, 16, v176
	v_and_b32_e32 v139, s5, v176
	v_lshlrev_b32_e32 v140, 16, v177
	v_and_b32_e32 v141, s5, v177
	v_pk_fma_f32 v[78:79], v[220:221], v[134:135], v[78:79] op_sel_hi:[0,1,1]
	v_pk_fma_f32 v[80:81], v[220:221], v[136:137], v[80:81] op_sel_hi:[0,1,1]
	v_pk_fma_f32 v[74:75], v[220:221], v[138:139], v[74:75] op_sel_hi:[0,1,1]
	v_pk_fma_f32 v[76:77], v[220:221], v[140:141], v[76:77] op_sel_hi:[0,1,1]
	v_pk_mul_f32 v[236:237], v[78:79], v[78:79]
	v_pk_fma_f32 v[236:237], v[80:81], v[80:81], v[236:237]
	v_pk_fma_f32 v[236:237], v[74:75], v[74:75], v[236:237]
	v_pk_fma_f32 v[236:237], v[76:77], v[76:77], v[236:237]
	v_cvt_pk_bf16_f32 v78, v78, v79
	v_cvt_pk_bf16_f32 v79, v80, v81
	v_cvt_pk_bf16_f32 v80, v74, v75
	v_cvt_pk_bf16_f32 v81, v76, v77
	ds_bpermute_b32 v78, v147, v78
	ds_bpermute_b32 v79, v147, v79
	ds_bpermute_b32 v80, v147, v80
	ds_bpermute_b32 v81, v147, v81
	s_waitcnt lgkmcnt(4)
	global_store_dwordx4 v[144:145], v[86:89], off offset:256
	v_lshl_add_u64 v[144:145], v[144:145], 0, s[98:99]
	s_waitcnt vmcnt(14)
	v_lshlrev_b32_e32 v134, 16, v178
	v_and_b32_e32 v135, s5, v178
	v_lshlrev_b32_e32 v136, 16, v179
	v_and_b32_e32 v137, s5, v179
	v_lshlrev_b32_e32 v138, 16, v180
	v_and_b32_e32 v139, s5, v180
	v_lshlrev_b32_e32 v140, 16, v181
	v_and_b32_e32 v141, s5, v181
	v_pk_fma_f32 v[70:71], v[220:221], v[134:135], v[70:71] op_sel_hi:[0,1,1]
	v_pk_fma_f32 v[72:73], v[220:221], v[136:137], v[72:73] op_sel_hi:[0,1,1]
	v_pk_fma_f32 v[66:67], v[220:221], v[138:139], v[66:67] op_sel_hi:[0,1,1]
	v_pk_fma_f32 v[68:69], v[220:221], v[140:141], v[68:69] op_sel_hi:[0,1,1]
	v_pk_fma_f32 v[236:237], v[70:71], v[70:71], v[236:237]
	v_pk_fma_f32 v[236:237], v[72:73], v[72:73], v[236:237]
	v_pk_fma_f32 v[236:237], v[66:67], v[66:67], v[236:237]
	v_pk_fma_f32 v[236:237], v[68:69], v[68:69], v[236:237]
	v_cvt_pk_bf16_f32 v70, v70, v71
	v_cvt_pk_bf16_f32 v71, v72, v73
	v_cvt_pk_bf16_f32 v72, v66, v67
	v_cvt_pk_bf16_f32 v73, v68, v69
	ds_bpermute_b32 v70, v147, v70
	ds_bpermute_b32 v71, v147, v71
	ds_bpermute_b32 v72, v147, v72
	ds_bpermute_b32 v73, v147, v73
	s_waitcnt lgkmcnt(4)
	global_store_dwordx4 v[144:145], v[78:81], off
	s_waitcnt vmcnt(14)
	v_lshlrev_b32_e32 v134, 16, v182
	v_and_b32_e32 v135, s5, v182
	v_lshlrev_b32_e32 v136, 16, v183
	v_and_b32_e32 v137, s5, v183
	v_lshlrev_b32_e32 v138, 16, v184
	v_and_b32_e32 v139, s5, v184
	v_lshlrev_b32_e32 v140, 16, v185
	v_and_b32_e32 v141, s5, v185
	v_pk_fma_f32 v[62:63], v[222:223], v[134:135], v[62:63] op_sel_hi:[0,1,1]
	v_pk_fma_f32 v[64:65], v[222:223], v[136:137], v[64:65] op_sel_hi:[0,1,1]
	v_pk_fma_f32 v[58:59], v[222:223], v[138:139], v[58:59] op_sel_hi:[0,1,1]
	v_pk_fma_f32 v[60:61], v[222:223], v[140:141], v[60:61] op_sel_hi:[0,1,1]
	v_pk_mul_f32 v[238:239], v[62:63], v[62:63]
	v_pk_fma_f32 v[238:239], v[64:65], v[64:65], v[238:239]
	v_pk_fma_f32 v[238:239], v[58:59], v[58:59], v[238:239]
	v_pk_fma_f32 v[238:239], v[60:61], v[60:61], v[238:239]
	v_cvt_pk_bf16_f32 v62, v62, v63
	v_cvt_pk_bf16_f32 v63, v64, v65
	v_cvt_pk_bf16_f32 v64, v58, v59
	v_cvt_pk_bf16_f32 v65, v60, v61
	ds_bpermute_b32 v62, v147, v62
	ds_bpermute_b32 v63, v147, v63
	ds_bpermute_b32 v64, v147, v64
	ds_bpermute_b32 v65, v147, v65
	s_waitcnt lgkmcnt(4)
	global_store_dwordx4 v[144:145], v[70:73], off offset:256
	v_lshl_add_u64 v[144:145], v[144:145], 0, s[100:101]
	s_waitcnt vmcnt(14)
	v_lshlrev_b32_e32 v134, 16, v186
	v_and_b32_e32 v135, s5, v186
	v_lshlrev_b32_e32 v136, 16, v187
	v_and_b32_e32 v137, s5, v187
	v_lshlrev_b32_e32 v138, 16, v188
	v_and_b32_e32 v139, s5, v188
	v_lshlrev_b32_e32 v140, 16, v189
	v_and_b32_e32 v141, s5, v189
	v_pk_fma_f32 v[54:55], v[222:223], v[134:135], v[54:55] op_sel_hi:[0,1,1]
	v_pk_fma_f32 v[56:57], v[222:223], v[136:137], v[56:57] op_sel_hi:[0,1,1]
	v_pk_fma_f32 v[50:51], v[222:223], v[138:139], v[50:51] op_sel_hi:[0,1,1]
	v_pk_fma_f32 v[52:53], v[222:223], v[140:141], v[52:53] op_sel_hi:[0,1,1]
	v_pk_fma_f32 v[238:239], v[54:55], v[54:55], v[238:239]
	v_pk_fma_f32 v[238:239], v[56:57], v[56:57], v[238:239]
	v_pk_fma_f32 v[238:239], v[50:51], v[50:51], v[238:239]
	v_pk_fma_f32 v[238:239], v[52:53], v[52:53], v[238:239]
	v_cvt_pk_bf16_f32 v54, v54, v55
	v_cvt_pk_bf16_f32 v55, v56, v57
	v_cvt_pk_bf16_f32 v56, v50, v51
	v_cvt_pk_bf16_f32 v57, v52, v53
	ds_bpermute_b32 v54, v147, v54
	ds_bpermute_b32 v55, v147, v55
	ds_bpermute_b32 v56, v147, v56
	ds_bpermute_b32 v57, v147, v57
	s_waitcnt lgkmcnt(4)
	global_store_dwordx4 v[144:145], v[62:65], off
	s_waitcnt vmcnt(14)
	v_lshlrev_b32_e32 v134, 16, v190
	v_and_b32_e32 v135, s5, v190
	v_lshlrev_b32_e32 v136, 16, v191
	v_and_b32_e32 v137, s5, v191
	v_lshlrev_b32_e32 v138, 16, v192
	v_and_b32_e32 v139, s5, v192
	v_lshlrev_b32_e32 v140, 16, v193
	v_and_b32_e32 v141, s5, v193
	v_pk_fma_f32 v[46:47], v[224:225], v[134:135], v[46:47] op_sel_hi:[0,1,1]
	v_pk_fma_f32 v[48:49], v[224:225], v[136:137], v[48:49] op_sel_hi:[0,1,1]
	v_pk_fma_f32 v[42:43], v[224:225], v[138:139], v[42:43] op_sel_hi:[0,1,1]
	v_pk_fma_f32 v[44:45], v[224:225], v[140:141], v[44:45] op_sel_hi:[0,1,1]
	v_pk_mul_f32 v[240:241], v[46:47], v[46:47]
	v_pk_fma_f32 v[240:241], v[48:49], v[48:49], v[240:241]
	v_pk_fma_f32 v[240:241], v[42:43], v[42:43], v[240:241]
	v_pk_fma_f32 v[240:241], v[44:45], v[44:45], v[240:241]
	v_cvt_pk_bf16_f32 v46, v46, v47
	v_cvt_pk_bf16_f32 v47, v48, v49
	v_cvt_pk_bf16_f32 v48, v42, v43
	v_cvt_pk_bf16_f32 v49, v44, v45
	ds_bpermute_b32 v46, v147, v46
	ds_bpermute_b32 v47, v147, v47
	ds_bpermute_b32 v48, v147, v48
	ds_bpermute_b32 v49, v147, v49
	s_waitcnt lgkmcnt(4)
	global_store_dwordx4 v[144:145], v[54:57], off offset:256
	v_lshl_add_u64 v[144:145], v[144:145], 0, s[98:99]
	s_waitcnt vmcnt(14)
	v_lshlrev_b32_e32 v134, 16, v194
	v_and_b32_e32 v135, s5, v194
	v_lshlrev_b32_e32 v136, 16, v195
	v_and_b32_e32 v137, s5, v195
	v_lshlrev_b32_e32 v138, 16, v196
	v_and_b32_e32 v139, s5, v196
	v_lshlrev_b32_e32 v140, 16, v197
	v_and_b32_e32 v141, s5, v197
	v_pk_fma_f32 v[38:39], v[224:225], v[134:135], v[38:39] op_sel_hi:[0,1,1]
	v_pk_fma_f32 v[40:41], v[224:225], v[136:137], v[40:41] op_sel_hi:[0,1,1]
	v_pk_fma_f32 v[34:35], v[224:225], v[138:139], v[34:35] op_sel_hi:[0,1,1]
	v_pk_fma_f32 v[36:37], v[224:225], v[140:141], v[36:37] op_sel_hi:[0,1,1]
	v_pk_fma_f32 v[240:241], v[38:39], v[38:39], v[240:241]
	v_pk_fma_f32 v[240:241], v[40:41], v[40:41], v[240:241]
	v_pk_fma_f32 v[240:241], v[34:35], v[34:35], v[240:241]
	v_pk_fma_f32 v[240:241], v[36:37], v[36:37], v[240:241]
	v_cvt_pk_bf16_f32 v38, v38, v39
	v_cvt_pk_bf16_f32 v39, v40, v41
	v_cvt_pk_bf16_f32 v40, v34, v35
	v_cvt_pk_bf16_f32 v41, v36, v37
	ds_bpermute_b32 v38, v147, v38
	ds_bpermute_b32 v39, v147, v39
	ds_bpermute_b32 v40, v147, v40
	ds_bpermute_b32 v41, v147, v41
	s_waitcnt lgkmcnt(4)
	global_store_dwordx4 v[144:145], v[46:49], off
	s_waitcnt vmcnt(14)
	v_lshlrev_b32_e32 v134, 16, v198
	v_and_b32_e32 v135, s5, v198
	v_lshlrev_b32_e32 v136, 16, v199
	v_and_b32_e32 v137, s5, v199
	v_lshlrev_b32_e32 v138, 16, v200
	v_and_b32_e32 v139, s5, v200
	v_lshlrev_b32_e32 v140, 16, v201
	v_and_b32_e32 v141, s5, v201
	v_pk_fma_f32 v[30:31], v[226:227], v[134:135], v[30:31] op_sel_hi:[0,1,1]
	v_pk_fma_f32 v[32:33], v[226:227], v[136:137], v[32:33] op_sel_hi:[0,1,1]
	v_pk_fma_f32 v[26:27], v[226:227], v[138:139], v[26:27] op_sel_hi:[0,1,1]
	v_pk_fma_f32 v[28:29], v[226:227], v[140:141], v[28:29] op_sel_hi:[0,1,1]
	v_pk_mul_f32 v[242:243], v[30:31], v[30:31]
	v_pk_fma_f32 v[242:243], v[32:33], v[32:33], v[242:243]
	v_pk_fma_f32 v[242:243], v[26:27], v[26:27], v[242:243]
	v_pk_fma_f32 v[242:243], v[28:29], v[28:29], v[242:243]
	v_cvt_pk_bf16_f32 v30, v30, v31
	v_cvt_pk_bf16_f32 v31, v32, v33
	v_cvt_pk_bf16_f32 v32, v26, v27
	v_cvt_pk_bf16_f32 v33, v28, v29
	ds_bpermute_b32 v30, v147, v30
	ds_bpermute_b32 v31, v147, v31
	ds_bpermute_b32 v32, v147, v32
	ds_bpermute_b32 v33, v147, v33
	s_waitcnt lgkmcnt(4)
	global_store_dwordx4 v[144:145], v[38:41], off offset:256
	v_lshl_add_u64 v[144:145], v[144:145], 0, s[98:99]
	s_waitcnt vmcnt(14)
	v_lshlrev_b32_e32 v134, 16, v202
	v_and_b32_e32 v135, s5, v202
	v_lshlrev_b32_e32 v136, 16, v203
	v_and_b32_e32 v137, s5, v203
	v_lshlrev_b32_e32 v138, 16, v204
	v_and_b32_e32 v139, s5, v204
	v_lshlrev_b32_e32 v140, 16, v205
	v_and_b32_e32 v141, s5, v205
	v_pk_fma_f32 v[22:23], v[226:227], v[134:135], v[22:23] op_sel_hi:[0,1,1]
	v_pk_fma_f32 v[24:25], v[226:227], v[136:137], v[24:25] op_sel_hi:[0,1,1]
	v_pk_fma_f32 v[18:19], v[226:227], v[138:139], v[18:19] op_sel_hi:[0,1,1]
	v_pk_fma_f32 v[20:21], v[226:227], v[140:141], v[20:21] op_sel_hi:[0,1,1]
	v_pk_fma_f32 v[242:243], v[22:23], v[22:23], v[242:243]
	v_pk_fma_f32 v[242:243], v[24:25], v[24:25], v[242:243]
	v_pk_fma_f32 v[242:243], v[18:19], v[18:19], v[242:243]
	v_pk_fma_f32 v[242:243], v[20:21], v[20:21], v[242:243]
	v_cvt_pk_bf16_f32 v22, v22, v23
	v_cvt_pk_bf16_f32 v23, v24, v25
	v_cvt_pk_bf16_f32 v24, v18, v19
	v_cvt_pk_bf16_f32 v25, v20, v21
	ds_bpermute_b32 v22, v147, v22
	ds_bpermute_b32 v23, v147, v23
	ds_bpermute_b32 v24, v147, v24
	ds_bpermute_b32 v25, v147, v25
	s_waitcnt lgkmcnt(4)
	global_store_dwordx4 v[144:145], v[30:33], off
	s_waitcnt vmcnt(14)
	v_lshlrev_b32_e32 v134, 16, v206
	v_and_b32_e32 v135, s5, v206
	v_lshlrev_b32_e32 v136, 16, v207
	v_and_b32_e32 v137, s5, v207
	v_lshlrev_b32_e32 v138, 16, v208
	v_and_b32_e32 v139, s5, v208
	v_lshlrev_b32_e32 v140, 16, v209
	v_and_b32_e32 v141, s5, v209
	v_pk_fma_f32 v[14:15], v[228:229], v[134:135], v[14:15] op_sel_hi:[0,1,1]
	v_pk_fma_f32 v[16:17], v[228:229], v[136:137], v[16:17] op_sel_hi:[0,1,1]
	v_pk_fma_f32 v[10:11], v[228:229], v[138:139], v[10:11] op_sel_hi:[0,1,1]
	v_pk_fma_f32 v[12:13], v[228:229], v[140:141], v[12:13] op_sel_hi:[0,1,1]
	v_pk_mul_f32 v[244:245], v[14:15], v[14:15]
	v_pk_fma_f32 v[244:245], v[16:17], v[16:17], v[244:245]
	v_pk_fma_f32 v[244:245], v[10:11], v[10:11], v[244:245]
	v_pk_fma_f32 v[244:245], v[12:13], v[12:13], v[244:245]
	v_cvt_pk_bf16_f32 v14, v14, v15
	v_cvt_pk_bf16_f32 v15, v16, v17
	v_cvt_pk_bf16_f32 v16, v10, v11
	v_cvt_pk_bf16_f32 v17, v12, v13
	ds_bpermute_b32 v14, v147, v14
	ds_bpermute_b32 v15, v147, v15
	ds_bpermute_b32 v16, v147, v16
	ds_bpermute_b32 v17, v147, v17
	s_waitcnt lgkmcnt(4)
	global_store_dwordx4 v[144:145], v[22:25], off offset:256
	v_lshl_add_u64 v[144:145], v[144:145], 0, s[98:99]
	s_waitcnt vmcnt(14)
	v_lshlrev_b32_e32 v134, 16, v210
	v_and_b32_e32 v135, s5, v210
	v_lshlrev_b32_e32 v136, 16, v211
	v_and_b32_e32 v137, s5, v211
	v_lshlrev_b32_e32 v138, 16, v212
	v_and_b32_e32 v139, s5, v212
	v_lshlrev_b32_e32 v140, 16, v213
	v_and_b32_e32 v141, s5, v213
	v_pk_fma_f32 v[6:7], v[228:229], v[134:135], v[6:7] op_sel_hi:[0,1,1]
	v_pk_fma_f32 v[8:9], v[228:229], v[136:137], v[8:9] op_sel_hi:[0,1,1]
	v_pk_fma_f32 v[2:3], v[228:229], v[138:139], v[2:3] op_sel_hi:[0,1,1]
	v_pk_fma_f32 v[4:5], v[228:229], v[140:141], v[4:5] op_sel_hi:[0,1,1]
	v_pk_fma_f32 v[244:245], v[6:7], v[6:7], v[244:245]
	v_pk_fma_f32 v[244:245], v[8:9], v[8:9], v[244:245]
	v_pk_fma_f32 v[244:245], v[2:3], v[2:3], v[244:245]
	v_pk_fma_f32 v[244:245], v[4:5], v[4:5], v[244:245]
	v_cvt_pk_bf16_f32 v6, v6, v7
	v_cvt_pk_bf16_f32 v7, v8, v9
	v_cvt_pk_bf16_f32 v8, v2, v3
	v_cvt_pk_bf16_f32 v9, v4, v5
	ds_bpermute_b32 v6, v147, v6
	ds_bpermute_b32 v7, v147, v7
	ds_bpermute_b32 v8, v147, v8
	ds_bpermute_b32 v9, v147, v9
	s_waitcnt lgkmcnt(4)
	global_store_dwordx4 v[144:145], v[14:17], off
	s_waitcnt lgkmcnt(0)
	global_store_dwordx4 v[144:145], v[6:9], off offset:256
	v_add_f32_e32 v230, v230, v231
	v_add_f32_e32 v232, v232, v233
	v_add_f32_e32 v234, v234, v235
	v_add_f32_e32 v236, v236, v237
	v_add_f32_e32 v238, v238, v239
	v_add_f32_e32 v240, v240, v241
	v_add_f32_e32 v242, v242, v243
	v_add_f32_e32 v244, v244, v245
	ds_bpermute_b32 v150, v148, v230
	ds_bpermute_b32 v151, v148, v232
	ds_bpermute_b32 v152, v148, v234
	ds_bpermute_b32 v153, v148, v236
	ds_bpermute_b32 v154, v148, v238
	ds_bpermute_b32 v155, v148, v240
	ds_bpermute_b32 v156, v148, v242
	ds_bpermute_b32 v157, v148, v244
	s_waitcnt lgkmcnt(0)
	v_add_f32_e32 v230, v230, v150
	v_add_f32_e32 v232, v232, v151
	v_add_f32_e32 v234, v234, v152
	v_add_f32_e32 v236, v236, v153
	v_add_f32_e32 v238, v238, v154
	v_add_f32_e32 v240, v240, v155
	v_add_f32_e32 v242, v242, v156
	v_add_f32_e32 v244, v244, v157
	ds_bpermute_b32 v150, v149, v230
	ds_bpermute_b32 v151, v149, v232
	ds_bpermute_b32 v152, v149, v234
	ds_bpermute_b32 v153, v149, v236
	ds_bpermute_b32 v154, v149, v238
	ds_bpermute_b32 v155, v149, v240
	ds_bpermute_b32 v156, v149, v242
	ds_bpermute_b32 v157, v149, v244
	s_waitcnt lgkmcnt(0)
	v_add_f32_e32 v230, v230, v150
	v_add_f32_e32 v232, v232, v151
	v_add_f32_e32 v234, v234, v152
	v_add_f32_e32 v236, v236, v153
	v_add_f32_e32 v238, v238, v154
	v_add_f32_e32 v240, v240, v155
	v_add_f32_e32 v242, v242, v156
	v_add_f32_e32 v244, v244, v157
	v_cmp_gt_u32_e32 vcc, 16, v248
	s_and_saveexec_b64 s[0:1], vcc
	ds_write_b32 v249, v230
	ds_write_b32 v249, v232 offset:256
	ds_write_b32 v249, v234 offset:512
	ds_write_b32 v249, v236 offset:768
	ds_write_b32 v249, v238 offset:2048
	ds_write_b32 v249, v240 offset:2304
	ds_write_b32 v249, v242 offset:2560
	ds_write_b32 v249, v244 offset:2816
	s_or_b64 exec, exec, s[0:1]
	s_nop 0
	s_waitcnt lgkmcnt(0)
	s_barrier
	s_andn2_b32 s49, s49, 63
	v_or_b32_e32 v1, s49, v248
	s_movk_i32 s0, 0x100
	v_cmp_gt_i32_e32 vcc, s0, v1
	s_and_saveexec_b64 s[0:1], vcc
	s_cbranch_execz .LBB0_1744
	v_lshl_add_u32 v2, v1, 4, 0
	ds_read_b128 v[2:5], v2
	v_add_u32_e32 v6, s4, v1
	s_waitcnt lgkmcnt(1)
	v_ashrrev_i32_e32 v7, 31, v6
	s_ashr_i32 s11, s10, 31
	s_waitcnt lgkmcnt(0)
	v_mov_b32_e32 v8, v3
	v_mov_b32_e32 v9, v4
	v_mov_b32_e32 v3, v5
	v_pk_add_f32 v[2:3], v[8:9], v[2:3]
	s_nop 0
	v_add_f32_e32 v1, v2, v3
	v_lshl_add_u64 v[2:3], v[6:7], 4, s[46:47]
	v_lshl_add_u64 v[2:3], s[10:11], 2, v[2:3]
	v_add_co_u32_e32 v2, vcc, 0x1d70000, v2
	s_nop 1
	v_addc_co_u32_e32 v3, vcc, 0, v3, vcc
	global_store_dword v[2:3], v1, off
